# v41 + fp8 K-loop MFMAs reordered within each group of 8 so consecutive MFMAs share an operand
# speedup vs baseline: 1.0081x; 1.0051x over previous
.LBB0_177:
	s_add_u32 s28, s4, s26
	s_addc_u32 s29, s5, s27
	s_add_u32 s30, s28, 0xe000100
	s_addc_u32 s31, s29, 0
	ds_read_b128 v[24:27], v252
	ds_read_b128 v[28:31], v253
	s_and_b64 s[28:29], s[34:35], exec
	ds_read_b128 v[16:19], v252 offset:2048
	ds_read_b128 v[20:23], v253 offset:2048
	s_cselect_b32 s29, s7, s31
	s_cselect_b32 s28, s6, s30
	s_add_u32 s61, s56, s26
	ds_read_b128 v[8:11], v252 offset:16384
	ds_read_b128 v[12:15], v253 offset:16384
	s_addc_u32 s62, s57, s27
	ds_read_b128 v[0:3], v252 offset:18432
	ds_read_b128 v[4:7], v253 offset:18432
	s_and_b64 s[30:31], s[34:35], exec
	s_cselect_b32 s31, s23, s62
	s_cselect_b32 s30, s22, s61
	s_add_u32 s61, s58, s26
	s_addc_u32 s62, s59, s27
	s_and_b64 s[34:35], s[34:35], exec
	s_cselect_b32 s35, s25, s62
	s_cselect_b32 s34, s24, s61
	s_add_u32 s100, s16, s26
	s_addc_u32 s101, s17, s27
	s_add_i32 m0, s37, 0xc000
	ds_read_b128 v[186:189], v206
	ds_read_b128 v[214:217], v206 offset:2048
	ds_read_b128 v[190:193], v207
	ds_read_b128 v[218:221], v207 offset:2048
	ds_read_b128 v[222:225], v206 offset:4096
	ds_read_b128 v[230:233], v206 offset:6144
	ds_read_b128 v[226:229], v207 offset:4096
	ds_read_b128 v[234:237], v207 offset:6144
	global_load_lds_dwordx4 v166, s[100:101]
	s_add_i32 m0, s37, 0xe000
	s_nop 0
	global_load_lds_dwordx4 v168, s[100:101]
	s_waitcnt vmcnt(8)
	s_waitcnt lgkmcnt(0)
	s_barrier
	s_setprio 1
	s_waitcnt lgkmcnt(0)
	v_mfma_f32_16x16x128_f8f6f4 v[156:159], v[24:31], v[186:193], v[156:159]
	v_mfma_f32_16x16x128_f8f6f4 v[152:155], v[16:23], v[186:193], v[152:155]
	v_mfma_f32_16x16x128_f8f6f4 v[136:139], v[16:23], v[214:221], v[136:139]
	v_mfma_f32_16x16x128_f8f6f4 v[144:147], v[24:31], v[214:221], v[144:147]
	v_mfma_f32_16x16x128_f8f6f4 v[128:131], v[24:31], v[222:229], v[128:131]
	v_mfma_f32_16x16x128_f8f6f4 v[120:123], v[16:23], v[222:229], v[120:123]
	v_mfma_f32_16x16x128_f8f6f4 v[104:107], v[16:23], v[230:237], v[104:107]
	v_mfma_f32_16x16x128_f8f6f4 v[112:115], v[24:31], v[230:237], v[112:115]
	v_mfma_f32_16x16x128_f8f6f4 v[148:151], v[8:15], v[186:193], v[148:151]
	v_mfma_f32_16x16x128_f8f6f4 v[140:143], v[0:7], v[186:193], v[140:143]
	v_mfma_f32_16x16x128_f8f6f4 v[124:127], v[0:7], v[214:221], v[124:127]
	v_mfma_f32_16x16x128_f8f6f4 v[132:135], v[8:15], v[214:221], v[132:135]
	v_mfma_f32_16x16x128_f8f6f4 v[116:119], v[8:15], v[222:229], v[116:119]
	v_mfma_f32_16x16x128_f8f6f4 v[108:111], v[0:7], v[222:229], v[108:111]
	v_mfma_f32_16x16x128_f8f6f4 v[96:99], v[0:7], v[230:237], v[96:99]
	v_mfma_f32_16x16x128_f8f6f4 v[100:103], v[8:15], v[230:237], v[100:103]
	s_setprio 0
	s_barrier
	s_add_i32 s61, s44, s36
	s_mov_b32 m0, s61
	ds_read_b128 v[214:217], v206 offset:16384
	ds_read_b128 v[222:225], v206 offset:18432
	ds_read_b128 v[218:221], v207 offset:16384
	ds_read_b128 v[226:229], v207 offset:18432
	ds_read_b128 v[230:233], v206 offset:20480
	ds_read_b128 v[238:241], v206 offset:22528
	ds_read_b128 v[234:237], v207 offset:20480
	ds_read_b128 v[242:245], v207 offset:22528
	global_load_lds_dwordx4 v160, s[30:31]
	s_add_i32 m0, s61, 0x2000
	s_add_i32 s98, s46, s36
	global_load_lds_dwordx4 v162, s[30:31]
	s_mov_b32 m0, s98
	s_nop 0
	global_load_lds_dwordx4 v160, s[34:35]
	s_add_i32 m0, s98, 0x2000
	v_mov_b32_e32 v173, v165
	global_load_lds_dwordx4 v162, s[34:35]
	s_waitcnt vmcnt(6)
	s_waitcnt lgkmcnt(0)
	s_barrier
	s_setprio 1
	s_waitcnt lgkmcnt(0)
	v_mfma_f32_16x16x128_f8f6f4 v[92:95], v[24:31], v[214:221], v[92:95]
	v_mfma_f32_16x16x128_f8f6f4 v[88:91], v[16:23], v[214:221], v[88:91]
	v_mfma_f32_16x16x128_f8f6f4 v[72:75], v[16:23], v[222:229], v[72:75]
	v_mfma_f32_16x16x128_f8f6f4 v[80:83], v[24:31], v[222:229], v[80:83]
	s_mov_b32 m0, s37
	v_mfma_f32_16x16x128_f8f6f4 v[64:67], v[24:31], v[230:237], v[64:67]
	global_load_lds_dwordx4 v164, s[28:29]
	v_mfma_f32_16x16x128_f8f6f4 v[56:59], v[16:23], v[230:237], v[56:59]
	v_mfma_f32_16x16x128_f8f6f4 v[40:43], v[16:23], v[238:245], v[40:43]
	v_mfma_f32_16x16x128_f8f6f4 v[48:51], v[24:31], v[238:245], v[48:51]
	v_mfma_f32_16x16x128_f8f6f4 v[84:87], v[8:15], v[214:221], v[84:87]
	s_mov_b32 m0, s38
	v_mfma_f32_16x16x128_f8f6f4 v[76:79], v[0:7], v[214:221], v[76:79]
	global_load_lds_dwordx4 v172, s[28:29]
	v_mfma_f32_16x16x128_f8f6f4 v[60:63], v[0:7], v[222:229], v[60:63]
	v_mfma_f32_16x16x128_f8f6f4 v[68:71], v[8:15], v[222:229], v[68:71]
	v_mfma_f32_16x16x128_f8f6f4 v[52:55], v[8:15], v[230:237], v[52:55]
	v_mfma_f32_16x16x128_f8f6f4 v[44:47], v[0:7], v[230:237], v[44:47]
	v_mfma_f32_16x16x128_f8f6f4 v[32:35], v[0:7], v[238:245], v[32:35]
	v_mfma_f32_16x16x128_f8f6f4 v[36:39], v[8:15], v[238:245], v[36:39]
	s_setprio 0
	s_barrier
	ds_read_b128 v[0:3], v252 offset:32768
	ds_read_b128 v[4:7], v253 offset:32768
	ds_read_b128 v[8:11], v252 offset:34816
	ds_read_b128 v[12:15], v253 offset:34816
	ds_read_b128 v[16:19], v252 offset:49152
	ds_read_b128 v[20:23], v253 offset:49152
	ds_read_b128 v[24:27], v252 offset:51200
	ds_read_b128 v[28:31], v253 offset:51200
	s_mov_b32 m0, s39
	ds_read_b128 v[214:217], v206 offset:32768
	ds_read_b128 v[222:225], v206 offset:34816
	ds_read_b128 v[218:221], v207 offset:32768
	ds_read_b128 v[226:229], v207 offset:34816
	ds_read_b128 v[230:233], v206 offset:36864
	ds_read_b128 v[238:241], v206 offset:38912
	ds_read_b128 v[234:237], v207 offset:36864
	ds_read_b128 v[242:245], v207 offset:38912
	global_load_lds_dwordx4 v184, s[28:29]
	s_mov_b32 m0, s40
	s_nop 0
	global_load_lds_dwordx4 v182, s[28:29]
	s_waitcnt vmcnt(8)
	s_waitcnt lgkmcnt(0)
	s_barrier
	s_setprio 1
	s_waitcnt lgkmcnt(0)
	v_mfma_f32_16x16x128_f8f6f4 v[156:159], v[0:7], v[214:221], v[156:159]
	v_mfma_f32_16x16x128_f8f6f4 v[152:155], v[8:15], v[214:221], v[152:155]
	v_mfma_f32_16x16x128_f8f6f4 v[136:139], v[8:15], v[222:229], v[136:139]
	v_mfma_f32_16x16x128_f8f6f4 v[144:147], v[0:7], v[222:229], v[144:147]
	v_mfma_f32_16x16x128_f8f6f4 v[128:131], v[0:7], v[230:237], v[128:131]
	v_mfma_f32_16x16x128_f8f6f4 v[120:123], v[8:15], v[230:237], v[120:123]
	v_mfma_f32_16x16x128_f8f6f4 v[104:107], v[8:15], v[238:245], v[104:107]
	v_mfma_f32_16x16x128_f8f6f4 v[112:115], v[0:7], v[238:245], v[112:115]
	v_mfma_f32_16x16x128_f8f6f4 v[148:151], v[16:23], v[214:221], v[148:151]
	v_mfma_f32_16x16x128_f8f6f4 v[140:143], v[24:31], v[214:221], v[140:143]
	v_mfma_f32_16x16x128_f8f6f4 v[124:127], v[24:31], v[222:229], v[124:127]
	v_mfma_f32_16x16x128_f8f6f4 v[132:135], v[16:23], v[222:229], v[132:135]
	v_mfma_f32_16x16x128_f8f6f4 v[116:119], v[16:23], v[230:237], v[116:119]
	v_mfma_f32_16x16x128_f8f6f4 v[108:111], v[24:31], v[230:237], v[108:111]
	v_mfma_f32_16x16x128_f8f6f4 v[96:99], v[24:31], v[238:245], v[96:99]
	v_mfma_f32_16x16x128_f8f6f4 v[100:103], v[16:23], v[238:245], v[100:103]
	s_setprio 0
	s_barrier
	s_add_i32 s99, s36, 0x17f80
	s_mov_b32 m0, s99
	ds_read_b128 v[214:217], v206 offset:49152
	ds_read_b128 v[222:225], v206 offset:51200
	ds_read_b128 v[218:221], v207 offset:49152
	ds_read_b128 v[226:229], v207 offset:51200
	ds_read_b128 v[230:233], v206 offset:53248
	ds_read_b128 v[238:241], v206 offset:55296
	ds_read_b128 v[234:237], v207 offset:53248
	ds_read_b128 v[242:245], v207 offset:55296
	global_load_lds_dwordx4 v160, s[30:31] offset:128
	s_add_i32 m0, s99, 0x2000
	s_add_i32 s99, s36, 0x1bf80
	global_load_lds_dwordx4 v162, s[30:31] offset:128
	s_mov_b32 m0, s99
	s_nop 0
	global_load_lds_dwordx4 v160, s[34:35] offset:128
	s_add_i32 m0, s99, 0x2000
	s_nop 0
	global_load_lds_dwordx4 v162, s[34:35] offset:128
	s_waitcnt vmcnt(6)
	s_waitcnt lgkmcnt(0)
	s_barrier
	s_setprio 1
	s_waitcnt lgkmcnt(0)
	v_mfma_f32_16x16x128_f8f6f4 v[92:95], v[0:7], v[214:221], v[92:95]
	v_mfma_f32_16x16x128_f8f6f4 v[88:91], v[8:15], v[214:221], v[88:91]
	v_mfma_f32_16x16x128_f8f6f4 v[72:75], v[8:15], v[222:229], v[72:75]
	v_mfma_f32_16x16x128_f8f6f4 v[80:83], v[0:7], v[222:229], v[80:83]
	s_add_i32 m0, s41, 0xffffff80
	v_mfma_f32_16x16x128_f8f6f4 v[64:67], v[0:7], v[230:237], v[64:67]
	global_load_lds_dwordx4 v164, s[28:29] offset:128
	v_mfma_f32_16x16x128_f8f6f4 v[56:59], v[8:15], v[230:237], v[56:59]
	v_mfma_f32_16x16x128_f8f6f4 v[40:43], v[8:15], v[238:245], v[40:43]
	v_mfma_f32_16x16x128_f8f6f4 v[48:51], v[0:7], v[238:245], v[48:51]
	v_mfma_f32_16x16x128_f8f6f4 v[84:87], v[16:23], v[214:221], v[84:87]
	s_add_i32 m0, s42, 0xffffff80
	v_mfma_f32_16x16x128_f8f6f4 v[76:79], v[24:31], v[214:221], v[76:79]
	global_load_lds_dwordx4 v172, s[28:29] offset:128
	v_mfma_f32_16x16x128_f8f6f4 v[60:63], v[24:31], v[222:229], v[60:63]
	v_mfma_f32_16x16x128_f8f6f4 v[68:71], v[16:23], v[222:229], v[68:71]
	v_mfma_f32_16x16x128_f8f6f4 v[52:55], v[16:23], v[230:237], v[52:55]
	v_mfma_f32_16x16x128_f8f6f4 v[44:47], v[24:31], v[230:237], v[44:47]
	v_mfma_f32_16x16x128_f8f6f4 v[32:35], v[24:31], v[238:245], v[32:35]
	v_mfma_f32_16x16x128_f8f6f4 v[36:39], v[16:23], v[238:245], v[36:39]
	s_setprio 0
	s_barrier
	s_add_i32 s60, s60, 2
	s_add_u32 s26, s26, 0x100
	s_addc_u32 s27, s27, 0
	s_cmp_gt_u32 s60, 5
	s_cbranch_scc1 .LBB0_180

.LBB0_590:
	s_add_u32 s36, s8, s4
	s_addc_u32 s37, s9, s5
	s_add_u32 s38, s36, 0xe000100
	s_addc_u32 s39, s37, 0
	ds_read_b128 v[24:27], v252
	ds_read_b128 v[28:31], v253
	s_and_b64 s[36:37], s[40:41], exec
	ds_read_b128 v[16:19], v252 offset:2048
	ds_read_b128 v[20:23], v253 offset:2048
	s_cselect_b32 s37, s11, s39
	s_cselect_b32 s36, s10, s38
	s_add_u32 s90, s27, s4
	ds_read_b128 v[8:11], v252 offset:16384
	ds_read_b128 v[12:15], v253 offset:16384
	s_addc_u32 s91, s86, s5
	ds_read_b128 v[0:3], v252 offset:18432
	ds_read_b128 v[4:7], v253 offset:18432
	s_and_b64 s[38:39], s[40:41], exec
	s_cselect_b32 s39, s29, s91
	s_cselect_b32 s38, s28, s90
	s_add_u32 s90, s87, s4
	s_addc_u32 s91, s88, s5
	s_and_b64 s[40:41], s[40:41], exec
	s_cselect_b32 s41, s31, s91
	s_cselect_b32 s40, s30, s90
	s_add_u32 s100, s18, s4
	s_addc_u32 s101, s19, s5
	s_add_i32 m0, s61, 0xc000
	ds_read_b128 v[182:185], v201
	ds_read_b128 v[210:213], v201 offset:2048
	ds_read_b128 v[186:189], v202
	ds_read_b128 v[214:217], v202 offset:2048
	ds_read_b128 v[218:221], v201 offset:4096
	ds_read_b128 v[226:229], v201 offset:6144
	ds_read_b128 v[222:225], v202 offset:4096
	ds_read_b128 v[230:233], v202 offset:6144
	global_load_lds_dwordx4 v170, s[100:101]
	s_add_i32 m0, s61, 0xe000
	s_nop 0
	global_load_lds_dwordx4 v168, s[100:101]
	s_waitcnt vmcnt(8)
	s_waitcnt lgkmcnt(0)
	s_barrier
	s_setprio 1
	s_waitcnt lgkmcnt(0)
	v_mfma_f32_16x16x128_f8f6f4 v[156:159], v[24:31], v[182:189], v[156:159]
	v_mfma_f32_16x16x128_f8f6f4 v[148:151], v[16:23], v[182:189], v[148:151]
	v_mfma_f32_16x16x128_f8f6f4 v[132:135], v[16:23], v[210:217], v[132:135]
	v_mfma_f32_16x16x128_f8f6f4 v[140:143], v[24:31], v[210:217], v[140:143]
	v_mfma_f32_16x16x128_f8f6f4 v[124:127], v[24:31], v[218:225], v[124:127]
	v_mfma_f32_16x16x128_f8f6f4 v[116:119], v[16:23], v[218:225], v[116:119]
	v_mfma_f32_16x16x128_f8f6f4 v[100:103], v[16:23], v[226:233], v[100:103]
	v_mfma_f32_16x16x128_f8f6f4 v[108:111], v[24:31], v[226:233], v[108:111]
	v_mfma_f32_16x16x128_f8f6f4 v[152:155], v[8:15], v[182:189], v[152:155]
	v_mfma_f32_16x16x128_f8f6f4 v[144:147], v[0:7], v[182:189], v[144:147]
	v_mfma_f32_16x16x128_f8f6f4 v[128:131], v[0:7], v[210:217], v[128:131]
	v_mfma_f32_16x16x128_f8f6f4 v[136:139], v[8:15], v[210:217], v[136:139]
	v_mfma_f32_16x16x128_f8f6f4 v[120:123], v[8:15], v[218:225], v[120:123]
	v_mfma_f32_16x16x128_f8f6f4 v[112:115], v[0:7], v[218:225], v[112:115]
	v_mfma_f32_16x16x128_f8f6f4 v[96:99], v[0:7], v[226:233], v[96:99]
	v_mfma_f32_16x16x128_f8f6f4 v[104:107], v[8:15], v[226:233], v[104:107]
	s_setprio 0
	s_barrier
	s_add_i32 s90, s72, s44
	s_mov_b32 m0, s90
	ds_read_b128 v[210:213], v201 offset:16384
	ds_read_b128 v[218:221], v201 offset:18432
	ds_read_b128 v[214:217], v202 offset:16384
	ds_read_b128 v[222:225], v202 offset:18432
	ds_read_b128 v[226:229], v201 offset:20480
	ds_read_b128 v[234:237], v201 offset:22528
	ds_read_b128 v[230:233], v202 offset:20480
	ds_read_b128 v[238:241], v202 offset:22528
	global_load_lds_dwordx4 v160, s[38:39]
	s_add_i32 m0, s90, 0x2000
	s_add_i32 s98, s74, s44
	global_load_lds_dwordx4 v162, s[38:39]
	s_mov_b32 m0, s98
	s_nop 0
	global_load_lds_dwordx4 v160, s[40:41]
	s_add_i32 m0, s98, 0x2000
	v_mov_b32_e32 v167, v165
	global_load_lds_dwordx4 v162, s[40:41]
	s_waitcnt vmcnt(6)
	s_waitcnt lgkmcnt(0)
	s_barrier
	s_setprio 1
	s_waitcnt lgkmcnt(0)
	v_mfma_f32_16x16x128_f8f6f4 v[92:95], v[24:31], v[210:217], v[92:95]
	v_mfma_f32_16x16x128_f8f6f4 v[84:87], v[16:23], v[210:217], v[84:87]
	v_mfma_f32_16x16x128_f8f6f4 v[68:71], v[16:23], v[218:225], v[68:71]
	v_mfma_f32_16x16x128_f8f6f4 v[76:79], v[24:31], v[218:225], v[76:79]
	s_mov_b32 m0, s61
	v_mfma_f32_16x16x128_f8f6f4 v[60:63], v[24:31], v[226:233], v[60:63]
	global_load_lds_dwordx4 v164, s[36:37]
	v_mfma_f32_16x16x128_f8f6f4 v[52:55], v[16:23], v[226:233], v[52:55]
	v_mfma_f32_16x16x128_f8f6f4 v[36:39], v[16:23], v[234:241], v[36:39]
	v_mfma_f32_16x16x128_f8f6f4 v[44:47], v[24:31], v[234:241], v[44:47]
	v_mfma_f32_16x16x128_f8f6f4 v[88:91], v[8:15], v[210:217], v[88:91]
	s_mov_b32 m0, s62
	v_mfma_f32_16x16x128_f8f6f4 v[80:83], v[0:7], v[210:217], v[80:83]
	global_load_lds_dwordx4 v166, s[36:37]
	v_mfma_f32_16x16x128_f8f6f4 v[64:67], v[0:7], v[218:225], v[64:67]
	v_mfma_f32_16x16x128_f8f6f4 v[72:75], v[8:15], v[218:225], v[72:75]
	v_mfma_f32_16x16x128_f8f6f4 v[56:59], v[8:15], v[226:233], v[56:59]
	v_mfma_f32_16x16x128_f8f6f4 v[48:51], v[0:7], v[226:233], v[48:51]
	v_mfma_f32_16x16x128_f8f6f4 v[32:35], v[0:7], v[234:241], v[32:35]
	v_mfma_f32_16x16x128_f8f6f4 v[40:43], v[8:15], v[234:241], v[40:43]
	s_setprio 0
	s_barrier
	ds_read_b128 v[0:3], v252 offset:32768
	ds_read_b128 v[4:7], v253 offset:32768
	ds_read_b128 v[8:11], v252 offset:34816
	ds_read_b128 v[12:15], v253 offset:34816
	ds_read_b128 v[16:19], v252 offset:49152
	ds_read_b128 v[20:23], v253 offset:49152
	ds_read_b128 v[24:27], v252 offset:51200
	ds_read_b128 v[28:31], v253 offset:51200
	s_mov_b32 m0, s63
	ds_read_b128 v[210:213], v201 offset:32768
	ds_read_b128 v[218:221], v201 offset:34816
	ds_read_b128 v[214:217], v202 offset:32768
	ds_read_b128 v[222:225], v202 offset:34816
	ds_read_b128 v[226:229], v201 offset:36864
	ds_read_b128 v[234:237], v201 offset:38912
	ds_read_b128 v[230:233], v202 offset:36864
	ds_read_b128 v[238:241], v202 offset:38912
	global_load_lds_dwordx4 v180, s[36:37]
	s_mov_b32 m0, s64
	s_nop 0
	global_load_lds_dwordx4 v178, s[36:37]
	s_waitcnt vmcnt(8)
	s_waitcnt lgkmcnt(0)
	s_barrier
	s_setprio 1
	s_waitcnt lgkmcnt(0)
	v_mfma_f32_16x16x128_f8f6f4 v[156:159], v[0:7], v[210:217], v[156:159]
	v_mfma_f32_16x16x128_f8f6f4 v[148:151], v[8:15], v[210:217], v[148:151]
	v_mfma_f32_16x16x128_f8f6f4 v[132:135], v[8:15], v[218:225], v[132:135]
	v_mfma_f32_16x16x128_f8f6f4 v[140:143], v[0:7], v[218:225], v[140:143]
	v_mfma_f32_16x16x128_f8f6f4 v[124:127], v[0:7], v[226:233], v[124:127]
	v_mfma_f32_16x16x128_f8f6f4 v[116:119], v[8:15], v[226:233], v[116:119]
	v_mfma_f32_16x16x128_f8f6f4 v[100:103], v[8:15], v[234:241], v[100:103]
	v_mfma_f32_16x16x128_f8f6f4 v[108:111], v[0:7], v[234:241], v[108:111]
	v_mfma_f32_16x16x128_f8f6f4 v[152:155], v[16:23], v[210:217], v[152:155]
	v_mfma_f32_16x16x128_f8f6f4 v[144:147], v[24:31], v[210:217], v[144:147]
	v_mfma_f32_16x16x128_f8f6f4 v[128:131], v[24:31], v[218:225], v[128:131]
	v_mfma_f32_16x16x128_f8f6f4 v[136:139], v[16:23], v[218:225], v[136:139]
	v_mfma_f32_16x16x128_f8f6f4 v[120:123], v[16:23], v[226:233], v[120:123]
	v_mfma_f32_16x16x128_f8f6f4 v[112:115], v[24:31], v[226:233], v[112:115]
	v_mfma_f32_16x16x128_f8f6f4 v[96:99], v[24:31], v[234:241], v[96:99]
	v_mfma_f32_16x16x128_f8f6f4 v[104:107], v[16:23], v[234:241], v[104:107]
	s_setprio 0
	s_barrier
	s_add_i32 s99, s44, 0x17f80
	s_mov_b32 m0, s99
	ds_read_b128 v[210:213], v201 offset:49152
	ds_read_b128 v[218:221], v201 offset:51200
	ds_read_b128 v[214:217], v202 offset:49152
	ds_read_b128 v[222:225], v202 offset:51200
	ds_read_b128 v[226:229], v201 offset:53248
	ds_read_b128 v[234:237], v201 offset:55296
	ds_read_b128 v[230:233], v202 offset:53248
	ds_read_b128 v[238:241], v202 offset:55296
	global_load_lds_dwordx4 v160, s[38:39] offset:128
	s_add_i32 m0, s99, 0x2000
	s_add_i32 s99, s44, 0x1bf80
	global_load_lds_dwordx4 v162, s[38:39] offset:128
	s_mov_b32 m0, s99
	s_nop 0
	global_load_lds_dwordx4 v160, s[40:41] offset:128
	s_add_i32 m0, s99, 0x2000
	s_nop 0
	global_load_lds_dwordx4 v162, s[40:41] offset:128
	s_waitcnt vmcnt(6)
	s_waitcnt lgkmcnt(0)
	s_barrier
	s_setprio 1
	s_waitcnt lgkmcnt(0)
	v_mfma_f32_16x16x128_f8f6f4 v[92:95], v[0:7], v[210:217], v[92:95]
	v_mfma_f32_16x16x128_f8f6f4 v[84:87], v[8:15], v[210:217], v[84:87]
	v_mfma_f32_16x16x128_f8f6f4 v[68:71], v[8:15], v[218:225], v[68:71]
	v_mfma_f32_16x16x128_f8f6f4 v[76:79], v[0:7], v[218:225], v[76:79]
	s_add_i32 m0, s65, 0xffffff80
	v_mfma_f32_16x16x128_f8f6f4 v[60:63], v[0:7], v[226:233], v[60:63]
	global_load_lds_dwordx4 v164, s[36:37] offset:128
	v_mfma_f32_16x16x128_f8f6f4 v[52:55], v[8:15], v[226:233], v[52:55]
	v_mfma_f32_16x16x128_f8f6f4 v[36:39], v[8:15], v[234:241], v[36:39]
	v_mfma_f32_16x16x128_f8f6f4 v[44:47], v[0:7], v[234:241], v[44:47]
	v_mfma_f32_16x16x128_f8f6f4 v[88:91], v[16:23], v[210:217], v[88:91]
	s_add_i32 m0, s66, 0xffffff80
	v_mfma_f32_16x16x128_f8f6f4 v[80:83], v[24:31], v[210:217], v[80:83]
	global_load_lds_dwordx4 v166, s[36:37] offset:128
	v_mfma_f32_16x16x128_f8f6f4 v[64:67], v[24:31], v[218:225], v[64:67]
	v_mfma_f32_16x16x128_f8f6f4 v[72:75], v[16:23], v[218:225], v[72:75]
	v_mfma_f32_16x16x128_f8f6f4 v[56:59], v[16:23], v[226:233], v[56:59]
	v_mfma_f32_16x16x128_f8f6f4 v[48:51], v[24:31], v[226:233], v[48:51]
	v_mfma_f32_16x16x128_f8f6f4 v[32:35], v[24:31], v[234:241], v[32:35]
	v_mfma_f32_16x16x128_f8f6f4 v[40:43], v[16:23], v[234:241], v[40:43]
	s_setprio 0
	s_barrier
	s_add_i32 s89, s89, 2
	s_add_u32 s4, s4, 0x100
	s_addc_u32 s5, s5, 0
	s_cmp_gt_u32 s89, 5
	s_cbranch_scc1 .LBB0_593

.LBB0_672:
	s_add_u32 s36, s6, s34
	s_addc_u32 s37, s7, s35
	s_add_u32 s38, s36, 0x12c00100
	s_addc_u32 s39, s37, 0
	ds_read_b128 v[24:27], v252
	ds_read_b128 v[28:31], v253
	s_and_b64 s[36:37], s[40:41], exec
	ds_read_b128 v[16:19], v252 offset:2048
	ds_read_b128 v[20:23], v253 offset:2048
	s_cselect_b32 s37, s9, s39
	s_cselect_b32 s36, s8, s38
	s_add_u32 s86, s27, s34
	ds_read_b128 v[8:11], v252 offset:16384
	ds_read_b128 v[12:15], v253 offset:16384
	s_addc_u32 s87, s82, s35
	ds_read_b128 v[0:3], v252 offset:18432
	ds_read_b128 v[4:7], v253 offset:18432
	s_and_b64 s[38:39], s[40:41], exec
	s_cselect_b32 s39, s29, s87
	s_cselect_b32 s38, s28, s86
	s_add_u32 s86, s83, s34
	s_addc_u32 s87, s84, s35
	s_and_b64 s[40:41], s[40:41], exec
	s_cselect_b32 s41, s31, s87
	s_cselect_b32 s40, s30, s86
	s_add_u32 s100, s16, s34
	s_addc_u32 s101, s17, s35
	s_add_i32 m0, s59, 0xc000
	ds_read_b128 v[186:189], v207
	ds_read_b128 v[216:219], v207 offset:2048
	ds_read_b128 v[190:193], v208
	ds_read_b128 v[220:223], v208 offset:2048
	ds_read_b128 v[224:227], v207 offset:4096
	ds_read_b128 v[232:235], v207 offset:6144
	ds_read_b128 v[228:231], v208 offset:4096
	ds_read_b128 v[236:239], v208 offset:6144
	global_load_lds_dwordx4 v166, s[100:101]
	s_add_i32 m0, s59, 0xe000
	s_nop 0
	global_load_lds_dwordx4 v168, s[100:101]
	s_waitcnt vmcnt(8)
	s_waitcnt lgkmcnt(0)
	s_barrier
	s_setprio 1
	s_waitcnt lgkmcnt(0)
	v_mfma_f32_16x16x128_f8f6f4 v[156:159], v[24:31], v[186:193], v[156:159]
	v_mfma_f32_16x16x128_f8f6f4 v[152:155], v[16:23], v[186:193], v[152:155]
	v_mfma_f32_16x16x128_f8f6f4 v[136:139], v[16:23], v[216:223], v[136:139]
	v_mfma_f32_16x16x128_f8f6f4 v[140:143], v[24:31], v[216:223], v[140:143]
	v_mfma_f32_16x16x128_f8f6f4 v[124:127], v[24:31], v[224:231], v[124:127]
	v_mfma_f32_16x16x128_f8f6f4 v[120:123], v[16:23], v[224:231], v[120:123]
	v_mfma_f32_16x16x128_f8f6f4 v[104:107], v[16:23], v[232:239], v[104:107]
	v_mfma_f32_16x16x128_f8f6f4 v[108:111], v[24:31], v[232:239], v[108:111]
	v_mfma_f32_16x16x128_f8f6f4 v[148:151], v[8:15], v[186:193], v[148:151]
	v_mfma_f32_16x16x128_f8f6f4 v[144:147], v[0:7], v[186:193], v[144:147]
	v_mfma_f32_16x16x128_f8f6f4 v[128:131], v[0:7], v[216:223], v[128:131]
	v_mfma_f32_16x16x128_f8f6f4 v[132:135], v[8:15], v[216:223], v[132:135]
	v_mfma_f32_16x16x128_f8f6f4 v[116:119], v[8:15], v[224:231], v[116:119]
	v_mfma_f32_16x16x128_f8f6f4 v[112:115], v[0:7], v[224:231], v[112:115]
	v_mfma_f32_16x16x128_f8f6f4 v[96:99], v[0:7], v[232:239], v[96:99]
	v_mfma_f32_16x16x128_f8f6f4 v[100:103], v[8:15], v[232:239], v[100:103]
	s_setprio 0
	s_barrier
	s_add_i32 s86, s69, s42
	s_mov_b32 m0, s86
	ds_read_b128 v[216:219], v207 offset:16384
	ds_read_b128 v[224:227], v207 offset:18432
	ds_read_b128 v[220:223], v208 offset:16384
	ds_read_b128 v[228:231], v208 offset:18432
	ds_read_b128 v[232:235], v207 offset:20480
	ds_read_b128 v[240:243], v207 offset:22528
	ds_read_b128 v[236:239], v208 offset:20480
	ds_read_b128 v[244:247], v208 offset:22528
	global_load_lds_dwordx4 v160, s[38:39]
	s_add_i32 m0, s86, 0x2000
	s_add_i32 s98, s71, s42
	global_load_lds_dwordx4 v162, s[38:39]
	s_mov_b32 m0, s98
	s_nop 0
	global_load_lds_dwordx4 v160, s[40:41]
	s_add_i32 m0, s98, 0x2000
	v_mov_b32_e32 v173, v165
	global_load_lds_dwordx4 v162, s[40:41]
	s_waitcnt vmcnt(6)
	s_waitcnt lgkmcnt(0)
	s_barrier
	s_setprio 1
	s_waitcnt lgkmcnt(0)
	v_mfma_f32_16x16x128_f8f6f4 v[92:95], v[24:31], v[216:223], v[92:95]
	v_mfma_f32_16x16x128_f8f6f4 v[88:91], v[16:23], v[216:223], v[88:91]
	v_mfma_f32_16x16x128_f8f6f4 v[72:75], v[16:23], v[224:231], v[72:75]
	v_mfma_f32_16x16x128_f8f6f4 v[76:79], v[24:31], v[224:231], v[76:79]
	s_mov_b32 m0, s59
	v_mfma_f32_16x16x128_f8f6f4 v[60:63], v[24:31], v[232:239], v[60:63]
	global_load_lds_dwordx4 v164, s[36:37]
	v_mfma_f32_16x16x128_f8f6f4 v[56:59], v[16:23], v[232:239], v[56:59]
	v_mfma_f32_16x16x128_f8f6f4 v[40:43], v[16:23], v[240:247], v[40:43]
	v_mfma_f32_16x16x128_f8f6f4 v[44:47], v[24:31], v[240:247], v[44:47]
	v_mfma_f32_16x16x128_f8f6f4 v[84:87], v[8:15], v[216:223], v[84:87]
	s_mov_b32 m0, s60
	v_mfma_f32_16x16x128_f8f6f4 v[80:83], v[0:7], v[216:223], v[80:83]
	global_load_lds_dwordx4 v172, s[36:37]
	v_mfma_f32_16x16x128_f8f6f4 v[64:67], v[0:7], v[224:231], v[64:67]
	v_mfma_f32_16x16x128_f8f6f4 v[68:71], v[8:15], v[224:231], v[68:71]
	v_mfma_f32_16x16x128_f8f6f4 v[52:55], v[8:15], v[232:239], v[52:55]
	v_mfma_f32_16x16x128_f8f6f4 v[48:51], v[0:7], v[232:239], v[48:51]
	v_mfma_f32_16x16x128_f8f6f4 v[32:35], v[0:7], v[240:247], v[32:35]
	v_mfma_f32_16x16x128_f8f6f4 v[36:39], v[8:15], v[240:247], v[36:39]
	s_setprio 0
	s_barrier
	ds_read_b128 v[0:3], v252 offset:32768
	ds_read_b128 v[4:7], v253 offset:32768
	ds_read_b128 v[8:11], v252 offset:34816
	ds_read_b128 v[12:15], v253 offset:34816
	ds_read_b128 v[16:19], v252 offset:49152
	ds_read_b128 v[20:23], v253 offset:49152
	ds_read_b128 v[24:27], v252 offset:51200
	ds_read_b128 v[28:31], v253 offset:51200
	s_mov_b32 m0, s61
	ds_read_b128 v[216:219], v207 offset:32768
	ds_read_b128 v[224:227], v207 offset:34816
	ds_read_b128 v[220:223], v208 offset:32768
	ds_read_b128 v[228:231], v208 offset:34816
	ds_read_b128 v[232:235], v207 offset:36864
	ds_read_b128 v[240:243], v207 offset:38912
	ds_read_b128 v[236:239], v208 offset:36864
	ds_read_b128 v[244:247], v208 offset:38912
	global_load_lds_dwordx4 v184, s[36:37]
	s_mov_b32 m0, s62
	s_nop 0
	global_load_lds_dwordx4 v182, s[36:37]
	s_waitcnt vmcnt(8)
	s_waitcnt lgkmcnt(0)
	s_barrier
	s_setprio 1
	s_waitcnt lgkmcnt(0)
	v_mfma_f32_16x16x128_f8f6f4 v[156:159], v[0:7], v[216:223], v[156:159]
	v_mfma_f32_16x16x128_f8f6f4 v[152:155], v[8:15], v[216:223], v[152:155]
	v_mfma_f32_16x16x128_f8f6f4 v[136:139], v[8:15], v[224:231], v[136:139]
	v_mfma_f32_16x16x128_f8f6f4 v[140:143], v[0:7], v[224:231], v[140:143]
	v_mfma_f32_16x16x128_f8f6f4 v[124:127], v[0:7], v[232:239], v[124:127]
	v_mfma_f32_16x16x128_f8f6f4 v[120:123], v[8:15], v[232:239], v[120:123]
	v_mfma_f32_16x16x128_f8f6f4 v[104:107], v[8:15], v[240:247], v[104:107]
	v_mfma_f32_16x16x128_f8f6f4 v[108:111], v[0:7], v[240:247], v[108:111]
	v_mfma_f32_16x16x128_f8f6f4 v[148:151], v[16:23], v[216:223], v[148:151]
	v_mfma_f32_16x16x128_f8f6f4 v[144:147], v[24:31], v[216:223], v[144:147]
	v_mfma_f32_16x16x128_f8f6f4 v[128:131], v[24:31], v[224:231], v[128:131]
	v_mfma_f32_16x16x128_f8f6f4 v[132:135], v[16:23], v[224:231], v[132:135]
	v_mfma_f32_16x16x128_f8f6f4 v[116:119], v[16:23], v[232:239], v[116:119]
	v_mfma_f32_16x16x128_f8f6f4 v[112:115], v[24:31], v[232:239], v[112:115]
	v_mfma_f32_16x16x128_f8f6f4 v[96:99], v[24:31], v[240:247], v[96:99]
	v_mfma_f32_16x16x128_f8f6f4 v[100:103], v[16:23], v[240:247], v[100:103]
	s_setprio 0
	s_barrier
	s_add_i32 s99, s42, 0x17f80
	s_mov_b32 m0, s99
	ds_read_b128 v[216:219], v207 offset:49152
	ds_read_b128 v[224:227], v207 offset:51200
	ds_read_b128 v[220:223], v208 offset:49152
	ds_read_b128 v[228:231], v208 offset:51200
	ds_read_b128 v[232:235], v207 offset:53248
	ds_read_b128 v[240:243], v207 offset:55296
	ds_read_b128 v[236:239], v208 offset:53248
	ds_read_b128 v[244:247], v208 offset:55296
	global_load_lds_dwordx4 v160, s[38:39] offset:128
	s_add_i32 m0, s99, 0x2000
	s_add_i32 s99, s42, 0x1bf80
	global_load_lds_dwordx4 v162, s[38:39] offset:128
	s_mov_b32 m0, s99
	s_nop 0
	global_load_lds_dwordx4 v160, s[40:41] offset:128
	s_add_i32 m0, s99, 0x2000
	s_nop 0
	global_load_lds_dwordx4 v162, s[40:41] offset:128
	s_waitcnt vmcnt(6)
	s_waitcnt lgkmcnt(0)
	s_barrier
	s_setprio 1
	s_waitcnt lgkmcnt(0)
	v_mfma_f32_16x16x128_f8f6f4 v[92:95], v[0:7], v[216:223], v[92:95]
	v_mfma_f32_16x16x128_f8f6f4 v[88:91], v[8:15], v[216:223], v[88:91]
	v_mfma_f32_16x16x128_f8f6f4 v[72:75], v[8:15], v[224:231], v[72:75]
	v_mfma_f32_16x16x128_f8f6f4 v[76:79], v[0:7], v[224:231], v[76:79]
	s_add_i32 m0, s63, 0xffffff80
	v_mfma_f32_16x16x128_f8f6f4 v[60:63], v[0:7], v[232:239], v[60:63]
	global_load_lds_dwordx4 v164, s[36:37] offset:128
	v_mfma_f32_16x16x128_f8f6f4 v[56:59], v[8:15], v[232:239], v[56:59]
	v_mfma_f32_16x16x128_f8f6f4 v[40:43], v[8:15], v[240:247], v[40:43]
	v_mfma_f32_16x16x128_f8f6f4 v[44:47], v[0:7], v[240:247], v[44:47]
	v_mfma_f32_16x16x128_f8f6f4 v[84:87], v[16:23], v[216:223], v[84:87]
	s_add_i32 m0, s64, 0xffffff80
	v_mfma_f32_16x16x128_f8f6f4 v[80:83], v[24:31], v[216:223], v[80:83]
	global_load_lds_dwordx4 v172, s[36:37] offset:128
	v_mfma_f32_16x16x128_f8f6f4 v[64:67], v[24:31], v[224:231], v[64:67]
	v_mfma_f32_16x16x128_f8f6f4 v[68:71], v[16:23], v[224:231], v[68:71]
	v_mfma_f32_16x16x128_f8f6f4 v[52:55], v[16:23], v[232:239], v[52:55]
	v_mfma_f32_16x16x128_f8f6f4 v[48:51], v[24:31], v[232:239], v[48:51]
	v_mfma_f32_16x16x128_f8f6f4 v[32:35], v[24:31], v[240:247], v[32:35]
	v_mfma_f32_16x16x128_f8f6f4 v[36:39], v[16:23], v[240:247], v[36:39]
	s_setprio 0
	s_barrier
	s_add_i32 s85, s85, 2
	s_add_u32 s34, s34, 0x100
	s_addc_u32 s35, s35, 0
	s_cmp_gt_u32 s85, 5
	s_cbranch_scc1 .LBB0_675

.LBB0_817:
	s_add_u32 s28, s10, s26
	s_addc_u32 s29, s11, s27
	s_add_u32 s30, s28, 0x38000100
	s_addc_u32 s31, s29, 0
	ds_read_b128 v[24:27], v252
	ds_read_b128 v[28:31], v253
	s_and_b64 s[28:29], s[34:35], exec
	ds_read_b128 v[16:19], v252 offset:2048
	ds_read_b128 v[20:23], v253 offset:2048
	s_cselect_b32 s29, s1, s31
	s_cselect_b32 s28, s0, s30
	s_add_u32 s61, s56, s26
	ds_read_b128 v[8:11], v252 offset:16384
	ds_read_b128 v[12:15], v253 offset:16384
	s_addc_u32 s62, s57, s27
	ds_read_b128 v[0:3], v252 offset:18432
	ds_read_b128 v[4:7], v253 offset:18432
	s_and_b64 s[30:31], s[34:35], exec
	s_cselect_b32 s31, s23, s62
	s_cselect_b32 s30, s22, s61
	s_add_u32 s61, s58, s26
	s_addc_u32 s62, s59, s27
	s_and_b64 s[34:35], s[34:35], exec
	s_cselect_b32 s35, s25, s62
	s_cselect_b32 s34, s24, s61
	s_add_u32 s100, s14, s26
	s_addc_u32 s101, s15, s27
	s_add_i32 m0, s37, 0xc000
	ds_read_b128 v[186:189], v207
	ds_read_b128 v[216:219], v207 offset:2048
	ds_read_b128 v[190:193], v208
	ds_read_b128 v[220:223], v208 offset:2048
	ds_read_b128 v[224:227], v207 offset:4096
	ds_read_b128 v[232:235], v207 offset:6144
	ds_read_b128 v[228:231], v208 offset:4096
	ds_read_b128 v[236:239], v208 offset:6144
	global_load_lds_dwordx4 v168, s[100:101]
	s_add_i32 m0, s37, 0xe000
	s_nop 0
	global_load_lds_dwordx4 v170, s[100:101]
	s_waitcnt vmcnt(8)
	s_waitcnt lgkmcnt(0)
	s_barrier
	s_setprio 1
	s_waitcnt lgkmcnt(0)
	v_mfma_f32_16x16x128_f8f6f4 v[156:159], v[24:31], v[186:193], v[156:159]
	v_mfma_f32_16x16x128_f8f6f4 v[152:155], v[16:23], v[186:193], v[152:155]
	v_mfma_f32_16x16x128_f8f6f4 v[136:139], v[16:23], v[216:223], v[136:139]
	v_mfma_f32_16x16x128_f8f6f4 v[140:143], v[24:31], v[216:223], v[140:143]
	v_mfma_f32_16x16x128_f8f6f4 v[124:127], v[24:31], v[224:231], v[124:127]
	v_mfma_f32_16x16x128_f8f6f4 v[120:123], v[16:23], v[224:231], v[120:123]
	v_mfma_f32_16x16x128_f8f6f4 v[104:107], v[16:23], v[232:239], v[104:107]
	v_mfma_f32_16x16x128_f8f6f4 v[108:111], v[24:31], v[232:239], v[108:111]
	v_mfma_f32_16x16x128_f8f6f4 v[148:151], v[8:15], v[186:193], v[148:151]
	v_mfma_f32_16x16x128_f8f6f4 v[144:147], v[0:7], v[186:193], v[144:147]
	v_mfma_f32_16x16x128_f8f6f4 v[128:131], v[0:7], v[216:223], v[128:131]
	v_mfma_f32_16x16x128_f8f6f4 v[132:135], v[8:15], v[216:223], v[132:135]
	v_mfma_f32_16x16x128_f8f6f4 v[116:119], v[8:15], v[224:231], v[116:119]
	v_mfma_f32_16x16x128_f8f6f4 v[112:115], v[0:7], v[224:231], v[112:115]
	v_mfma_f32_16x16x128_f8f6f4 v[96:99], v[0:7], v[232:239], v[96:99]
	v_mfma_f32_16x16x128_f8f6f4 v[100:103], v[8:15], v[232:239], v[100:103]
	s_setprio 0
	s_barrier
	s_add_i32 s61, s44, s36
	s_mov_b32 m0, s61
	ds_read_b128 v[216:219], v207 offset:16384
	ds_read_b128 v[224:227], v207 offset:18432
	ds_read_b128 v[220:223], v208 offset:16384
	ds_read_b128 v[228:231], v208 offset:18432
	ds_read_b128 v[232:235], v207 offset:20480
	ds_read_b128 v[240:243], v207 offset:22528
	ds_read_b128 v[236:239], v208 offset:20480
	ds_read_b128 v[244:247], v208 offset:22528
	global_load_lds_dwordx4 v160, s[30:31]
	s_add_i32 m0, s61, 0x2000
	s_add_i32 s98, s46, s36
	global_load_lds_dwordx4 v162, s[30:31]
	s_mov_b32 m0, s98
	s_nop 0
	global_load_lds_dwordx4 v160, s[34:35]
	s_add_i32 m0, s98, 0x2000
	v_mov_b32_e32 v167, v165
	global_load_lds_dwordx4 v162, s[34:35]
	s_waitcnt vmcnt(6)
	s_waitcnt lgkmcnt(0)
	s_barrier
	s_setprio 1
	s_waitcnt lgkmcnt(0)
	v_mfma_f32_16x16x128_f8f6f4 v[92:95], v[24:31], v[216:223], v[92:95]
	v_mfma_f32_16x16x128_f8f6f4 v[88:91], v[16:23], v[216:223], v[88:91]
	v_mfma_f32_16x16x128_f8f6f4 v[72:75], v[16:23], v[224:231], v[72:75]
	v_mfma_f32_16x16x128_f8f6f4 v[76:79], v[24:31], v[224:231], v[76:79]
	s_mov_b32 m0, s37
	v_mfma_f32_16x16x128_f8f6f4 v[60:63], v[24:31], v[232:239], v[60:63]
	global_load_lds_dwordx4 v164, s[28:29]
	v_mfma_f32_16x16x128_f8f6f4 v[56:59], v[16:23], v[232:239], v[56:59]
	v_mfma_f32_16x16x128_f8f6f4 v[40:43], v[16:23], v[240:247], v[40:43]
	v_mfma_f32_16x16x128_f8f6f4 v[44:47], v[24:31], v[240:247], v[44:47]
	v_mfma_f32_16x16x128_f8f6f4 v[84:87], v[8:15], v[216:223], v[84:87]
	s_mov_b32 m0, s38
	v_mfma_f32_16x16x128_f8f6f4 v[80:83], v[0:7], v[216:223], v[80:83]
	global_load_lds_dwordx4 v166, s[28:29]
	v_mfma_f32_16x16x128_f8f6f4 v[64:67], v[0:7], v[224:231], v[64:67]
	v_mfma_f32_16x16x128_f8f6f4 v[68:71], v[8:15], v[224:231], v[68:71]
	v_mfma_f32_16x16x128_f8f6f4 v[52:55], v[8:15], v[232:239], v[52:55]
	v_mfma_f32_16x16x128_f8f6f4 v[48:51], v[0:7], v[232:239], v[48:51]
	v_mfma_f32_16x16x128_f8f6f4 v[32:35], v[0:7], v[240:247], v[32:35]
	v_mfma_f32_16x16x128_f8f6f4 v[36:39], v[8:15], v[240:247], v[36:39]
	s_setprio 0
	s_barrier
	ds_read_b128 v[0:3], v252 offset:32768
	ds_read_b128 v[4:7], v253 offset:32768
	ds_read_b128 v[8:11], v252 offset:34816
	ds_read_b128 v[12:15], v253 offset:34816
	ds_read_b128 v[16:19], v252 offset:49152
	ds_read_b128 v[20:23], v253 offset:49152
	ds_read_b128 v[24:27], v252 offset:51200
	ds_read_b128 v[28:31], v253 offset:51200
	s_mov_b32 m0, s39
	ds_read_b128 v[216:219], v207 offset:32768
	ds_read_b128 v[224:227], v207 offset:34816
	ds_read_b128 v[220:223], v208 offset:32768
	ds_read_b128 v[228:231], v208 offset:34816
	ds_read_b128 v[232:235], v207 offset:36864
	ds_read_b128 v[240:243], v207 offset:38912
	ds_read_b128 v[236:239], v208 offset:36864
	ds_read_b128 v[244:247], v208 offset:38912
	global_load_lds_dwordx4 v184, s[28:29]
	s_mov_b32 m0, s40
	s_nop 0
	global_load_lds_dwordx4 v182, s[28:29]
	s_waitcnt vmcnt(8)
	s_waitcnt lgkmcnt(0)
	s_barrier
	s_setprio 1
	s_waitcnt lgkmcnt(0)
	v_mfma_f32_16x16x128_f8f6f4 v[156:159], v[0:7], v[216:223], v[156:159]
	v_mfma_f32_16x16x128_f8f6f4 v[152:155], v[8:15], v[216:223], v[152:155]
	v_mfma_f32_16x16x128_f8f6f4 v[136:139], v[8:15], v[224:231], v[136:139]
	v_mfma_f32_16x16x128_f8f6f4 v[140:143], v[0:7], v[224:231], v[140:143]
	v_mfma_f32_16x16x128_f8f6f4 v[124:127], v[0:7], v[232:239], v[124:127]
	v_mfma_f32_16x16x128_f8f6f4 v[120:123], v[8:15], v[232:239], v[120:123]
	v_mfma_f32_16x16x128_f8f6f4 v[104:107], v[8:15], v[240:247], v[104:107]
	v_mfma_f32_16x16x128_f8f6f4 v[108:111], v[0:7], v[240:247], v[108:111]
	v_mfma_f32_16x16x128_f8f6f4 v[148:151], v[16:23], v[216:223], v[148:151]
	v_mfma_f32_16x16x128_f8f6f4 v[144:147], v[24:31], v[216:223], v[144:147]
	v_mfma_f32_16x16x128_f8f6f4 v[128:131], v[24:31], v[224:231], v[128:131]
	v_mfma_f32_16x16x128_f8f6f4 v[132:135], v[16:23], v[224:231], v[132:135]
	v_mfma_f32_16x16x128_f8f6f4 v[116:119], v[16:23], v[232:239], v[116:119]
	v_mfma_f32_16x16x128_f8f6f4 v[112:115], v[24:31], v[232:239], v[112:115]
	v_mfma_f32_16x16x128_f8f6f4 v[96:99], v[24:31], v[240:247], v[96:99]
	v_mfma_f32_16x16x128_f8f6f4 v[100:103], v[16:23], v[240:247], v[100:103]
	s_setprio 0
	s_barrier
	s_add_i32 s99, s36, 0x17f80
	s_mov_b32 m0, s99
	ds_read_b128 v[216:219], v207 offset:49152
	ds_read_b128 v[224:227], v207 offset:51200
	ds_read_b128 v[220:223], v208 offset:49152
	ds_read_b128 v[228:231], v208 offset:51200
	ds_read_b128 v[232:235], v207 offset:53248
	ds_read_b128 v[240:243], v207 offset:55296
	ds_read_b128 v[236:239], v208 offset:53248
	ds_read_b128 v[244:247], v208 offset:55296
	global_load_lds_dwordx4 v160, s[30:31] offset:128
	s_add_i32 m0, s99, 0x2000
	s_add_i32 s99, s36, 0x1bf80
	global_load_lds_dwordx4 v162, s[30:31] offset:128
	s_mov_b32 m0, s99
	s_nop 0
	global_load_lds_dwordx4 v160, s[34:35] offset:128
	s_add_i32 m0, s99, 0x2000
	s_nop 0
	global_load_lds_dwordx4 v162, s[34:35] offset:128
	s_waitcnt vmcnt(6)
	s_waitcnt lgkmcnt(0)
	s_barrier
	s_setprio 1
	s_waitcnt lgkmcnt(0)
	v_mfma_f32_16x16x128_f8f6f4 v[92:95], v[0:7], v[216:223], v[92:95]
	v_mfma_f32_16x16x128_f8f6f4 v[88:91], v[8:15], v[216:223], v[88:91]
	v_mfma_f32_16x16x128_f8f6f4 v[72:75], v[8:15], v[224:231], v[72:75]
	v_mfma_f32_16x16x128_f8f6f4 v[76:79], v[0:7], v[224:231], v[76:79]
	s_add_i32 m0, s41, 0xffffff80
	v_mfma_f32_16x16x128_f8f6f4 v[60:63], v[0:7], v[232:239], v[60:63]
	global_load_lds_dwordx4 v164, s[28:29] offset:128
	v_mfma_f32_16x16x128_f8f6f4 v[56:59], v[8:15], v[232:239], v[56:59]
	v_mfma_f32_16x16x128_f8f6f4 v[40:43], v[8:15], v[240:247], v[40:43]
	v_mfma_f32_16x16x128_f8f6f4 v[44:47], v[0:7], v[240:247], v[44:47]
	v_mfma_f32_16x16x128_f8f6f4 v[84:87], v[16:23], v[216:223], v[84:87]
	s_add_i32 m0, s42, 0xffffff80
	v_mfma_f32_16x16x128_f8f6f4 v[80:83], v[24:31], v[216:223], v[80:83]
	global_load_lds_dwordx4 v166, s[28:29] offset:128
	v_mfma_f32_16x16x128_f8f6f4 v[64:67], v[24:31], v[224:231], v[64:67]
	v_mfma_f32_16x16x128_f8f6f4 v[68:71], v[16:23], v[224:231], v[68:71]
	v_mfma_f32_16x16x128_f8f6f4 v[52:55], v[16:23], v[232:239], v[52:55]
	v_mfma_f32_16x16x128_f8f6f4 v[48:51], v[24:31], v[232:239], v[48:51]
	v_mfma_f32_16x16x128_f8f6f4 v[32:35], v[24:31], v[240:247], v[32:35]
	v_mfma_f32_16x16x128_f8f6f4 v[36:39], v[16:23], v[240:247], v[36:39]
	s_setprio 0
	s_barrier
	s_add_i32 s60, s60, 2
	s_add_u32 s26, s26, 0x100
	s_addc_u32 s27, s27, 0
	s_cmp_gt_u32 s60, 5
	s_cbranch_scc1 .LBB0_820

.LBB0_1549:
	s_add_u32 s26, s4, s24
	s_addc_u32 s27, s5, s25
	s_add_u32 s28, s26, 0x28000100
	s_addc_u32 s29, s27, 0
	ds_read_b128 v[24:27], v252
	ds_read_b128 v[28:31], v253
	s_and_b64 s[26:27], s[30:31], exec
	ds_read_b128 v[16:19], v252 offset:2048
	ds_read_b128 v[20:23], v253 offset:2048
	s_cselect_b32 s27, s7, s29
	s_cselect_b32 s26, s6, s28
	s_add_u32 s63, s58, s24
	ds_read_b128 v[8:11], v252 offset:16384
	ds_read_b128 v[12:15], v253 offset:16384
	s_addc_u32 s64, s59, s25
	ds_read_b128 v[0:3], v252 offset:18432
	ds_read_b128 v[4:7], v253 offset:18432
	s_and_b64 s[28:29], s[30:31], exec
	s_cselect_b32 s29, s21, s64
	s_cselect_b32 s28, s20, s63
	s_add_u32 s63, s60, s24
	s_addc_u32 s64, s61, s25
	s_and_b64 s[30:31], s[30:31], exec
	s_cselect_b32 s31, s23, s64
	s_cselect_b32 s30, s22, s63
	s_add_u32 s100, s14, s24
	s_addc_u32 s101, s15, s25
	s_add_i32 m0, s35, 0xc000
	ds_read_b128 v[186:189], v206
	ds_read_b128 v[214:217], v206 offset:2048
	ds_read_b128 v[190:193], v207
	ds_read_b128 v[218:221], v207 offset:2048
	ds_read_b128 v[222:225], v206 offset:4096
	ds_read_b128 v[230:233], v206 offset:6144
	ds_read_b128 v[226:229], v207 offset:4096
	ds_read_b128 v[234:237], v207 offset:6144
	global_load_lds_dwordx4 v168, s[100:101]
	s_add_i32 m0, s35, 0xe000
	s_nop 0
	global_load_lds_dwordx4 v170, s[100:101]
	s_waitcnt vmcnt(8)
	s_waitcnt lgkmcnt(0)
	s_barrier
	s_setprio 1
	s_waitcnt lgkmcnt(0)
	v_mfma_f32_16x16x128_f8f6f4 v[156:159], v[24:31], v[186:193], v[156:159]
	v_mfma_f32_16x16x128_f8f6f4 v[152:155], v[16:23], v[186:193], v[152:155]
	v_mfma_f32_16x16x128_f8f6f4 v[136:139], v[16:23], v[214:221], v[136:139]
	v_mfma_f32_16x16x128_f8f6f4 v[144:147], v[24:31], v[214:221], v[144:147]
	v_mfma_f32_16x16x128_f8f6f4 v[124:127], v[24:31], v[222:229], v[124:127]
	v_mfma_f32_16x16x128_f8f6f4 v[120:123], v[16:23], v[222:229], v[120:123]
	v_mfma_f32_16x16x128_f8f6f4 v[104:107], v[16:23], v[230:237], v[104:107]
	v_mfma_f32_16x16x128_f8f6f4 v[112:115], v[24:31], v[230:237], v[112:115]
	v_mfma_f32_16x16x128_f8f6f4 v[148:151], v[8:15], v[186:193], v[148:151]
	v_mfma_f32_16x16x128_f8f6f4 v[140:143], v[0:7], v[186:193], v[140:143]
	v_mfma_f32_16x16x128_f8f6f4 v[128:131], v[0:7], v[214:221], v[128:131]
	v_mfma_f32_16x16x128_f8f6f4 v[132:135], v[8:15], v[214:221], v[132:135]
	v_mfma_f32_16x16x128_f8f6f4 v[116:119], v[8:15], v[222:229], v[116:119]
	v_mfma_f32_16x16x128_f8f6f4 v[108:111], v[0:7], v[222:229], v[108:111]
	v_mfma_f32_16x16x128_f8f6f4 v[96:99], v[0:7], v[230:237], v[96:99]
	v_mfma_f32_16x16x128_f8f6f4 v[100:103], v[8:15], v[230:237], v[100:103]
	s_setprio 0
	s_barrier
	s_add_i32 s63, s46, s34
	s_mov_b32 m0, s63
	ds_read_b128 v[214:217], v206 offset:16384
	ds_read_b128 v[222:225], v206 offset:18432
	ds_read_b128 v[218:221], v207 offset:16384
	ds_read_b128 v[226:229], v207 offset:18432
	ds_read_b128 v[230:233], v206 offset:20480
	ds_read_b128 v[238:241], v206 offset:22528
	ds_read_b128 v[234:237], v207 offset:20480
	ds_read_b128 v[242:245], v207 offset:22528
	global_load_lds_dwordx4 v160, s[28:29]
	s_add_i32 m0, s63, 0x2000
	s_add_i32 s98, s48, s34
	global_load_lds_dwordx4 v162, s[28:29]
	s_mov_b32 m0, s98
	s_nop 0
	global_load_lds_dwordx4 v160, s[30:31]
	s_add_i32 m0, s98, 0x2000
	v_mov_b32_e32 v167, v165
	global_load_lds_dwordx4 v162, s[30:31]
	s_waitcnt vmcnt(6)
	s_waitcnt lgkmcnt(0)
	s_barrier
	s_setprio 1
	s_waitcnt lgkmcnt(0)
	v_mfma_f32_16x16x128_f8f6f4 v[92:95], v[24:31], v[214:221], v[92:95]
	v_mfma_f32_16x16x128_f8f6f4 v[88:91], v[16:23], v[214:221], v[88:91]
	v_mfma_f32_16x16x128_f8f6f4 v[72:75], v[16:23], v[222:229], v[72:75]
	v_mfma_f32_16x16x128_f8f6f4 v[80:83], v[24:31], v[222:229], v[80:83]
	s_mov_b32 m0, s35
	v_mfma_f32_16x16x128_f8f6f4 v[60:63], v[24:31], v[230:237], v[60:63]
	global_load_lds_dwordx4 v164, s[26:27]
	v_mfma_f32_16x16x128_f8f6f4 v[56:59], v[16:23], v[230:237], v[56:59]
	v_mfma_f32_16x16x128_f8f6f4 v[40:43], v[16:23], v[238:245], v[40:43]
	v_mfma_f32_16x16x128_f8f6f4 v[48:51], v[24:31], v[238:245], v[48:51]
	v_mfma_f32_16x16x128_f8f6f4 v[84:87], v[8:15], v[214:221], v[84:87]
	s_mov_b32 m0, s36
	v_mfma_f32_16x16x128_f8f6f4 v[76:79], v[0:7], v[214:221], v[76:79]
	global_load_lds_dwordx4 v166, s[26:27]
	v_mfma_f32_16x16x128_f8f6f4 v[64:67], v[0:7], v[222:229], v[64:67]
	v_mfma_f32_16x16x128_f8f6f4 v[68:71], v[8:15], v[222:229], v[68:71]
	v_mfma_f32_16x16x128_f8f6f4 v[52:55], v[8:15], v[230:237], v[52:55]
	v_mfma_f32_16x16x128_f8f6f4 v[44:47], v[0:7], v[230:237], v[44:47]
	v_mfma_f32_16x16x128_f8f6f4 v[32:35], v[0:7], v[238:245], v[32:35]
	v_mfma_f32_16x16x128_f8f6f4 v[36:39], v[8:15], v[238:245], v[36:39]
	s_setprio 0
	s_barrier
	ds_read_b128 v[0:3], v252 offset:32768
	ds_read_b128 v[4:7], v253 offset:32768
	ds_read_b128 v[8:11], v252 offset:34816
	ds_read_b128 v[12:15], v253 offset:34816
	ds_read_b128 v[16:19], v252 offset:49152
	ds_read_b128 v[20:23], v253 offset:49152
	ds_read_b128 v[24:27], v252 offset:51200
	ds_read_b128 v[28:31], v253 offset:51200
	s_mov_b32 m0, s37
	ds_read_b128 v[214:217], v206 offset:32768
	ds_read_b128 v[222:225], v206 offset:34816
	ds_read_b128 v[218:221], v207 offset:32768
	ds_read_b128 v[226:229], v207 offset:34816
	ds_read_b128 v[230:233], v206 offset:36864
	ds_read_b128 v[238:241], v206 offset:38912
	ds_read_b128 v[234:237], v207 offset:36864
	ds_read_b128 v[242:245], v207 offset:38912
	global_load_lds_dwordx4 v184, s[26:27]
	s_mov_b32 m0, s38
	s_nop 0
	global_load_lds_dwordx4 v182, s[26:27]
	s_waitcnt vmcnt(8)
	s_waitcnt lgkmcnt(0)
	s_barrier
	s_setprio 1
	s_waitcnt lgkmcnt(0)
	v_mfma_f32_16x16x128_f8f6f4 v[156:159], v[0:7], v[214:221], v[156:159]
	v_mfma_f32_16x16x128_f8f6f4 v[152:155], v[8:15], v[214:221], v[152:155]
	v_mfma_f32_16x16x128_f8f6f4 v[136:139], v[8:15], v[222:229], v[136:139]
	v_mfma_f32_16x16x128_f8f6f4 v[144:147], v[0:7], v[222:229], v[144:147]
	v_mfma_f32_16x16x128_f8f6f4 v[124:127], v[0:7], v[230:237], v[124:127]
	v_mfma_f32_16x16x128_f8f6f4 v[120:123], v[8:15], v[230:237], v[120:123]
	v_mfma_f32_16x16x128_f8f6f4 v[104:107], v[8:15], v[238:245], v[104:107]
	v_mfma_f32_16x16x128_f8f6f4 v[112:115], v[0:7], v[238:245], v[112:115]
	v_mfma_f32_16x16x128_f8f6f4 v[148:151], v[16:23], v[214:221], v[148:151]
	v_mfma_f32_16x16x128_f8f6f4 v[140:143], v[24:31], v[214:221], v[140:143]
	v_mfma_f32_16x16x128_f8f6f4 v[128:131], v[24:31], v[222:229], v[128:131]
	v_mfma_f32_16x16x128_f8f6f4 v[132:135], v[16:23], v[222:229], v[132:135]
	v_mfma_f32_16x16x128_f8f6f4 v[116:119], v[16:23], v[230:237], v[116:119]
	v_mfma_f32_16x16x128_f8f6f4 v[108:111], v[24:31], v[230:237], v[108:111]
	v_mfma_f32_16x16x128_f8f6f4 v[96:99], v[24:31], v[238:245], v[96:99]
	v_mfma_f32_16x16x128_f8f6f4 v[100:103], v[16:23], v[238:245], v[100:103]
	s_setprio 0
	s_barrier
	s_add_i32 s99, s34, 0x17f80
	s_mov_b32 m0, s99
	ds_read_b128 v[214:217], v206 offset:49152
	ds_read_b128 v[222:225], v206 offset:51200
	ds_read_b128 v[218:221], v207 offset:49152
	ds_read_b128 v[226:229], v207 offset:51200
	ds_read_b128 v[230:233], v206 offset:53248
	ds_read_b128 v[238:241], v206 offset:55296
	ds_read_b128 v[234:237], v207 offset:53248
	ds_read_b128 v[242:245], v207 offset:55296
	global_load_lds_dwordx4 v160, s[28:29] offset:128
	s_add_i32 m0, s99, 0x2000
	s_add_i32 s99, s34, 0x1bf80
	global_load_lds_dwordx4 v162, s[28:29] offset:128
	s_mov_b32 m0, s99
	s_nop 0
	global_load_lds_dwordx4 v160, s[30:31] offset:128
	s_add_i32 m0, s99, 0x2000
	s_nop 0
	global_load_lds_dwordx4 v162, s[30:31] offset:128
	s_waitcnt vmcnt(6)
	s_waitcnt lgkmcnt(0)
	s_barrier
	s_setprio 1
	s_waitcnt lgkmcnt(0)
	v_mfma_f32_16x16x128_f8f6f4 v[92:95], v[0:7], v[214:221], v[92:95]
	v_mfma_f32_16x16x128_f8f6f4 v[88:91], v[8:15], v[214:221], v[88:91]
	v_mfma_f32_16x16x128_f8f6f4 v[72:75], v[8:15], v[222:229], v[72:75]
	v_mfma_f32_16x16x128_f8f6f4 v[80:83], v[0:7], v[222:229], v[80:83]
	s_add_i32 m0, s41, 0xffffff80
	v_mfma_f32_16x16x128_f8f6f4 v[60:63], v[0:7], v[230:237], v[60:63]
	global_load_lds_dwordx4 v164, s[26:27] offset:128
	v_mfma_f32_16x16x128_f8f6f4 v[56:59], v[8:15], v[230:237], v[56:59]
	v_mfma_f32_16x16x128_f8f6f4 v[40:43], v[8:15], v[238:245], v[40:43]
	v_mfma_f32_16x16x128_f8f6f4 v[48:51], v[0:7], v[238:245], v[48:51]
	v_mfma_f32_16x16x128_f8f6f4 v[84:87], v[16:23], v[214:221], v[84:87]
	s_add_i32 m0, s42, 0xffffff80
	v_mfma_f32_16x16x128_f8f6f4 v[76:79], v[24:31], v[214:221], v[76:79]
	global_load_lds_dwordx4 v166, s[26:27] offset:128
	v_mfma_f32_16x16x128_f8f6f4 v[64:67], v[24:31], v[222:229], v[64:67]
	v_mfma_f32_16x16x128_f8f6f4 v[68:71], v[16:23], v[222:229], v[68:71]
	v_mfma_f32_16x16x128_f8f6f4 v[52:55], v[16:23], v[230:237], v[52:55]
	v_mfma_f32_16x16x128_f8f6f4 v[44:47], v[24:31], v[230:237], v[44:47]
	v_mfma_f32_16x16x128_f8f6f4 v[32:35], v[24:31], v[238:245], v[32:35]
	v_mfma_f32_16x16x128_f8f6f4 v[36:39], v[16:23], v[238:245], v[36:39]
	s_setprio 0
	s_barrier
	s_add_i32 s62, s62, 2
	s_add_u32 s24, s24, 0x100
	s_addc_u32 s25, s25, 0
	s_cmp_gt_u32 s62, 29
	s_cbranch_scc1 .LBB0_1552
